# indexer tile: selection-layout address in byte units (v_and_or), per-head weight copies hoisted out of the loop
# baseline (speedup 1.0000x reference)
.LBB0_541:
	s_andn2_b64 vcc, exec, s[6:7]
	s_cbranch_vccnz .LBB0_890
	s_sub_i32 s5, s78, s1
	v_readlane_b32 s6, v255, 48
	s_add_i32 s5, s6, s5
	s_ashr_i32 s6, s5, 31
	s_lshr_b32 s6, s6, 25
	s_lshl_b32 s17, s5, 4
	s_add_i32 s6, s5, s6
	s_bfe_i32 s5, s5, 0x1001b
	s_lshr_b32 s5, s5, 21
	s_add_i32 s5, s17, s5
	s_and_b32 s5, s5, 0xfffff800
	s_sub_i32 s20, s17, s5
	s_ashr_i32 s42, s6, 7
	s_and_b32 s12, s20, 0xffffffc0
	s_add_i32 s18, s12, 64
	s_ashr_i32 s43, s42, 31
	v_and_b32_e32 v71, 15, v146
	v_lshrrev_b32_e32 v49, 4, v245
	s_cmpk_lt_i32 s12, 0x100
	v_lshlrev_b32_e32 v74, 2, v71
	s_brev_b32 s30, 1
	s_cbranch_scc1 .LBB0_558
	s_lshr_b32 s19, s18, 4
	s_cmp_ge_i32 s4, s19
	s_cbranch_scc1 .LBB0_558
	v_or_b32_e32 v2, s17, v71
	v_mov_b64_e32 v[0:1], s[88:89]
	v_mad_i64_i32 v[0:1], s[6:7], v2, s10, v[0:1]
	v_add_co_u32_e32 v2, vcc, 0x2000, v0
	s_mov_b64 s[6:7], 0x1500
	s_nop 0
	v_addc_co_u32_e32 v3, vcc, 0, v1, vcc
	global_load_dwordx2 v[192:193], v[2:3], off offset:896
	s_lshr_b32 s21, s18, 5
	v_cvt_f32_u32_e32 v32, s21
	s_sub_i32 s24, 0, s21
	v_lshlrev_b32_e32 v34, 2, v49
	v_mov_b32_e32 v33, v48
	v_rcp_iflag_f32_e32 v32, v32
	v_lshl_add_u32 v75, v71, 13, 0
	v_mul_f32_e32 v32, 0x4f7ffffe, v32
	v_cvt_u32_f32_e32 v32, v32
	v_lshlrev_b32_e32 v2, 4, v49
	v_mov_b32_e32 v3, v48
	v_lshl_add_u64 v[28:29], v[0:1], 0, v[2:3]
	v_lshl_add_u64 v[24:25], v[28:29], 0, s[6:7]
	global_load_dwordx4 v[0:3], v[24:25], off offset:448
	global_load_dwordx4 v[4:7], v[24:25], off offset:384
	global_load_dwordx4 v[8:11], v[24:25], off offset:320
	global_load_dwordx4 v[12:15], v[24:25], off offset:256
	global_load_dwordx4 v[16:19], v[24:25], off offset:192
	global_load_dwordx4 v[20:23], v[24:25], off offset:128
	s_nop 0
	global_load_dwordx4 v[24:27], v[24:25], off offset:64
	v_add_co_u32_e32 v28, vcc, s16, v28
	v_readfirstlane_b32 s5, v32
	s_nop 0
	v_addc_co_u32_e32 v29, vcc, 0, v29, vcc
	global_load_dwordx4 v[28:31], v[28:29], off offset:1280
	s_waitcnt vmcnt(8)
	v_and_b32_e32 v195, 0xffff0000, v192
	v_lshlrev_b32_e32 v194, 16, v192
	v_pk_mul_f32 v[66:67], v[194:195], 0.5 op_sel_hi:[1,0]
	v_and_b32_e32 v195, 0xffff0000, v193
	v_lshlrev_b32_e32 v194, 16, v193
	v_pk_mul_f32 v[68:69], v[194:195], 0.5 op_sel_hi:[1,0]
	s_mul_i32 s6, s24, s5
	s_mul_hi_u32 s6, s5, s6
	s_add_i32 s5, s5, s6
	s_mul_hi_u32 s5, s5, -1
	s_mul_i32 s6, s5, s21
	s_not_b32 s6, s6
	s_add_i32 s7, s5, 1
	s_sub_i32 s8, s6, s21
	s_cmp_ge_u32 s6, s21
	s_cselect_b32 s5, s7, s5
	s_cselect_b32 s6, s8, s6
	s_add_i32 s7, s5, 1
	s_cmp_ge_u32 s6, s21
	s_cselect_b32 s5, s7, s5
	s_add_i32 s25, s5, 1
	s_lshl_b32 s28, s4, 4
	s_lshl_b32 s5, s4, 9
	v_lshlrev_b32_e32 v32, 7, v49
	v_or3_b32 v70, s5, v32, v74
	s_add_i32 s5, s28, 0x180
	v_or_b32_e32 v77, s5, v34
	s_ashr_i32 s5, s4, 31
	s_lshl_b64 s[6:7], s[42:43], 18
	s_sub_i32 s26, 0xffffffc1, s12
	s_lshl_b64 s[8:9], s[4:5], 11
	s_add_u32 s5, s6, s8
	s_addc_u32 s7, s7, s9
	v_readlane_b32 s6, v255, 56
	s_add_u32 s6, s6, s5
	v_readlane_b32 s5, v255, 57
	v_or_b32_e32 v76, s28, v34
	v_lshlrev_b32_e32 v32, 4, v245
	s_addc_u32 s7, s5, s7
	s_add_i32 s5, s28, 0x100
	s_addk_i32 s28, 0x80
	v_lshl_add_u64 v[72:73], s[6:7], 0, v[32:33]
	v_or_b32_e32 v78, s5, v34
	v_or_b32_e32 v79, s28, v34
	s_mov_b32 s5, s4
	v_add_co_u32_e32 v138, vcc, 0xffff4000, v72
	s_nop 1
	v_addc_co_u32_e32 v139, vcc, -1, v73, vcc
	global_load_dwordx4 v[62:65], v[138:139], off offset:-1024
	global_load_dwordx4 v[58:61], v[138:139], off
	s_add_i32 s28, s5, 8
	s_mov_b32 s29, 0xffff4000
	s_cmp_lt_i32 s28, s19
	s_cselect_b32 s28, 0xffff8000, s29
	s_mov_b32 s29, -1
	v_mov_b32_e32 v139, s29
	v_add_co_u32_e32 v138, vcc, s28, v72
	s_nop 1
	v_addc_co_u32_e32 v139, vcc, v139, v73, vcc
	global_load_dwordx4 v[44:47], v[138:139], off offset:-1024
	global_load_dwordx4 v[54:57], v[138:139], off
	s_add_i32 s28, s5, 16
	s_mov_b32 s29, 0xffff4000
	s_cmp_lt_i32 s28, s19
	s_cselect_b32 s28, 0xffffc000, s29
	s_mov_b32 s29, -1
	v_mov_b32_e32 v139, s29
	v_add_co_u32_e32 v138, vcc, s28, v72
	s_nop 1
	v_addc_co_u32_e32 v139, vcc, v139, v73, vcc
	global_load_dwordx4 v[40:43], v[138:139], off offset:-1024
	global_load_dwordx4 v[50:53], v[138:139], off
	s_add_i32 s28, s5, 24
	s_mov_b32 s29, 0xffff4000
	s_cmp_lt_i32 s28, s19
	s_cselect_b32 s28, 0, s29
	s_cselect_b32 s29, 0, -1
	v_mov_b32_e32 v139, s29
	v_add_co_u32_e32 v138, vcc, s28, v72
	s_nop 1
	v_addc_co_u32_e32 v139, vcc, v139, v73, vcc
	global_load_dwordx4 v[32:35], v[138:139], off offset:-1024
	global_load_dwordx4 v[36:39], v[138:139], off
	v_mov_b32_e32 v140, v67
	v_mov_b32_e32 v142, v69
	v_mov_b32_e32 v144, 0x1ffc
	s_branch .LBB0_546

.LBB0_546:
	s_add_i32 s28, s5, 32
	s_cmp_lt_i32 s28, s19
	s_cbranch_scc0 .Lmy_ix_last
	s_waitcnt vmcnt(6)
	v_mfma_f32_16x16x32_bf16 v[100:103], v[62:65], v[28:31], 0
	v_mfma_f32_16x16x32_bf16 v[104:107], v[62:65], v[20:23], 0
	v_mfma_f32_16x16x32_bf16 v[108:111], v[62:65], v[12:15], 0
	v_mfma_f32_16x16x32_bf16 v[112:115], v[62:65], v[4:7], 0
	v_mfma_f32_16x16x32_bf16 v[100:103], v[58:61], v[24:27], v[100:103]
	v_mfma_f32_16x16x32_bf16 v[104:107], v[58:61], v[16:19], v[104:107]
	v_mfma_f32_16x16x32_bf16 v[108:111], v[58:61], v[8:11], v[108:111]
	v_mfma_f32_16x16x32_bf16 v[112:115], v[58:61], v[0:3], v[112:115]
	s_add_i32 s28, s5, 32
	s_mov_b32 s29, 0xffff4000
	s_cmp_lt_i32 s28, s19
	s_cselect_b32 s28, 0x4000, s29
	s_cselect_b32 s29, 0, -1
	v_mov_b32_e32 v139, s29
	v_add_co_u32_e32 v138, vcc, s28, v72
	s_nop 1
	v_addc_co_u32_e32 v139, vcc, v139, v73, vcc
	global_load_dwordx4 v[62:65], v[138:139], off offset:-1024
	global_load_dwordx4 v[58:61], v[138:139], off
	v_mul_hi_u32 v129, s25, v76
	v_mad_i32_i24 v130, v129, s24, v76
	v_lshlrev_b32_e32 v128, 2, v129
	v_lshl_add_u32 v131, v130, 7, v128
	v_lshl_add_u32 v131, v74, 2, v131
	v_add_u32_e32 v133, 2, v130
	v_cmp_eq_u32_e32 vcc, s21, v133
	v_lshl_add_u32 v133, v74, 2, v128
	v_add_u32_e32 v133, 4, v133
	v_add_u32_e32 v132, 0x100, v131
	v_and_or_b32 v134, v131, v144, v75
	v_cndmask_b32_e32 v132, v132, v133, vcc
	v_add_u32_e32 v128, 0x80, v131
	v_and_or_b32 v135, v128, v144, v75
	v_and_or_b32 v136, v132, v144, v75
	v_add_u32_e32 v128, 0x80, v132
	v_and_or_b32 v137, v128, v144, v75
	v_max_f32_e32 v100, 0, v100
	v_max_f32_e32 v101, 0, v101
	v_max_f32_e32 v102, 0, v102
	v_max_f32_e32 v103, 0, v103
	v_max_f32_e32 v104, 0, v104
	v_max_f32_e32 v105, 0, v105
	v_max_f32_e32 v106, 0, v106
	v_max_f32_e32 v107, 0, v107
	v_max_f32_e32 v108, 0, v108
	v_max_f32_e32 v109, 0, v109
	v_max_f32_e32 v110, 0, v110
	v_max_f32_e32 v111, 0, v111
	v_max_f32_e32 v112, 0, v112
	v_max_f32_e32 v113, 0, v113
	v_max_f32_e32 v114, 0, v114
	v_max_f32_e32 v115, 0, v115
	v_pk_mul_f32 v[120:121], v[100:101], v[66:67] op_sel_hi:[1,0]
	v_pk_add_f32 v[120:121], v[120:121], 0 op_sel_hi:[1,0]
	v_pk_mul_f32 v[116:117], v[104:105], v[140:141] op_sel_hi:[1,0]
	v_pk_add_f32 v[120:121], v[120:121], v[116:117]
	v_pk_mul_f32 v[116:117], v[108:109], v[68:69] op_sel_hi:[1,0]
	v_pk_add_f32 v[120:121], v[120:121], v[116:117]
	v_pk_mul_f32 v[116:117], v[112:113], v[142:143] op_sel_hi:[1,0]
	v_pk_add_f32 v[120:121], v[120:121], v[116:117]
	v_pk_mul_f32 v[122:123], v[102:103], v[66:67] op_sel_hi:[1,0]
	v_pk_add_f32 v[122:123], v[122:123], 0 op_sel_hi:[1,0]
	v_pk_mul_f32 v[118:119], v[106:107], v[140:141] op_sel_hi:[1,0]
	v_pk_add_f32 v[122:123], v[122:123], v[118:119]
	v_pk_mul_f32 v[118:119], v[110:111], v[68:69] op_sel_hi:[1,0]
	v_pk_add_f32 v[122:123], v[122:123], v[118:119]
	v_pk_mul_f32 v[118:119], v[114:115], v[142:143] op_sel_hi:[1,0]
	v_pk_add_f32 v[122:123], v[122:123], v[118:119]
	v_ashrrev_i32_e32 v128, 31, v120
	v_bitop3_b32 v124, v120, v128, s30 bitop3:0x1e
	ds_write_b32 v134, v124
	v_ashrrev_i32_e32 v128, 31, v121
	v_bitop3_b32 v125, v121, v128, s30 bitop3:0x1e
	ds_write_b32 v135, v125
	v_ashrrev_i32_e32 v128, 31, v122
	v_bitop3_b32 v126, v122, v128, s30 bitop3:0x1e
	ds_write_b32 v136, v126
	v_ashrrev_i32_e32 v128, 31, v123
	v_bitop3_b32 v127, v123, v128, s30 bitop3:0x1e
	ds_write_b32 v137, v127
	s_waitcnt vmcnt(6)
	v_mfma_f32_16x16x32_bf16 v[100:103], v[44:47], v[28:31], 0
	v_mfma_f32_16x16x32_bf16 v[104:107], v[44:47], v[20:23], 0
	v_mfma_f32_16x16x32_bf16 v[108:111], v[44:47], v[12:15], 0
	v_mfma_f32_16x16x32_bf16 v[112:115], v[44:47], v[4:7], 0
	v_mfma_f32_16x16x32_bf16 v[100:103], v[54:57], v[24:27], v[100:103]
	v_mfma_f32_16x16x32_bf16 v[104:107], v[54:57], v[16:19], v[104:107]
	v_mfma_f32_16x16x32_bf16 v[108:111], v[54:57], v[8:11], v[108:111]
	v_mfma_f32_16x16x32_bf16 v[112:115], v[54:57], v[0:3], v[112:115]
	s_add_i32 s28, s5, 40
	s_mov_b32 s29, 0xffff4000
	s_cmp_lt_i32 s28, s19
	s_cselect_b32 s28, 0x8000, s29
	s_cselect_b32 s29, 0, -1
	v_mov_b32_e32 v139, s29
	v_add_co_u32_e32 v138, vcc, s28, v72
	s_nop 1
	v_addc_co_u32_e32 v139, vcc, v139, v73, vcc
	global_load_dwordx4 v[44:47], v[138:139], off offset:-1024
	global_load_dwordx4 v[54:57], v[138:139], off
	v_mul_hi_u32 v129, s25, v79
	v_mad_i32_i24 v130, v129, s24, v79
	v_lshlrev_b32_e32 v128, 2, v129
	v_lshl_add_u32 v131, v130, 7, v128
	v_lshl_add_u32 v131, v74, 2, v131
	v_add_u32_e32 v133, 2, v130
	v_cmp_eq_u32_e32 vcc, s21, v133
	v_lshl_add_u32 v133, v74, 2, v128
	v_add_u32_e32 v133, 4, v133
	v_add_u32_e32 v132, 0x100, v131
	v_and_or_b32 v134, v131, v144, v75
	v_cndmask_b32_e32 v132, v132, v133, vcc
	v_add_u32_e32 v128, 0x80, v131
	v_and_or_b32 v135, v128, v144, v75
	v_and_or_b32 v136, v132, v144, v75
	v_add_u32_e32 v128, 0x80, v132
	v_and_or_b32 v137, v128, v144, v75
	v_max_f32_e32 v100, 0, v100
	v_max_f32_e32 v101, 0, v101
	v_max_f32_e32 v102, 0, v102
	v_max_f32_e32 v103, 0, v103
	v_max_f32_e32 v104, 0, v104
	v_max_f32_e32 v105, 0, v105
	v_max_f32_e32 v106, 0, v106
	v_max_f32_e32 v107, 0, v107
	v_max_f32_e32 v108, 0, v108
	v_max_f32_e32 v109, 0, v109
	v_max_f32_e32 v110, 0, v110
	v_max_f32_e32 v111, 0, v111
	v_max_f32_e32 v112, 0, v112
	v_max_f32_e32 v113, 0, v113
	v_max_f32_e32 v114, 0, v114
	v_max_f32_e32 v115, 0, v115
	v_pk_mul_f32 v[120:121], v[100:101], v[66:67] op_sel_hi:[1,0]
	v_pk_add_f32 v[120:121], v[120:121], 0 op_sel_hi:[1,0]
	v_pk_mul_f32 v[116:117], v[104:105], v[140:141] op_sel_hi:[1,0]
	v_pk_add_f32 v[120:121], v[120:121], v[116:117]
	v_pk_mul_f32 v[116:117], v[108:109], v[68:69] op_sel_hi:[1,0]
	v_pk_add_f32 v[120:121], v[120:121], v[116:117]
	v_pk_mul_f32 v[116:117], v[112:113], v[142:143] op_sel_hi:[1,0]
	v_pk_add_f32 v[120:121], v[120:121], v[116:117]
	v_pk_mul_f32 v[122:123], v[102:103], v[66:67] op_sel_hi:[1,0]
	v_pk_add_f32 v[122:123], v[122:123], 0 op_sel_hi:[1,0]
	v_pk_mul_f32 v[118:119], v[106:107], v[140:141] op_sel_hi:[1,0]
	v_pk_add_f32 v[122:123], v[122:123], v[118:119]
	v_pk_mul_f32 v[118:119], v[110:111], v[68:69] op_sel_hi:[1,0]
	v_pk_add_f32 v[122:123], v[122:123], v[118:119]
	v_pk_mul_f32 v[118:119], v[114:115], v[142:143] op_sel_hi:[1,0]
	v_pk_add_f32 v[122:123], v[122:123], v[118:119]
	v_ashrrev_i32_e32 v128, 31, v120
	v_bitop3_b32 v124, v120, v128, s30 bitop3:0x1e
	ds_write_b32 v134, v124
	v_ashrrev_i32_e32 v128, 31, v121
	v_bitop3_b32 v125, v121, v128, s30 bitop3:0x1e
	ds_write_b32 v135, v125
	v_ashrrev_i32_e32 v128, 31, v122
	v_bitop3_b32 v126, v122, v128, s30 bitop3:0x1e
	ds_write_b32 v136, v126
	v_ashrrev_i32_e32 v128, 31, v123
	v_bitop3_b32 v127, v123, v128, s30 bitop3:0x1e
	ds_write_b32 v137, v127
	s_waitcnt vmcnt(6)
	v_mfma_f32_16x16x32_bf16 v[100:103], v[40:43], v[28:31], 0
	v_mfma_f32_16x16x32_bf16 v[104:107], v[40:43], v[20:23], 0
	v_mfma_f32_16x16x32_bf16 v[108:111], v[40:43], v[12:15], 0
	v_mfma_f32_16x16x32_bf16 v[112:115], v[40:43], v[4:7], 0
	v_mfma_f32_16x16x32_bf16 v[100:103], v[50:53], v[24:27], v[100:103]
	v_mfma_f32_16x16x32_bf16 v[104:107], v[50:53], v[16:19], v[104:107]
	v_mfma_f32_16x16x32_bf16 v[108:111], v[50:53], v[8:11], v[108:111]
	v_mfma_f32_16x16x32_bf16 v[112:115], v[50:53], v[0:3], v[112:115]
	s_add_i32 s28, s5, 48
	s_mov_b32 s29, 0xffff4000
	s_cmp_lt_i32 s28, s19
	s_cselect_b32 s28, 0xc000, s29
	s_cselect_b32 s29, 0, -1
	v_mov_b32_e32 v139, s29
	v_add_co_u32_e32 v138, vcc, s28, v72
	s_nop 1
	v_addc_co_u32_e32 v139, vcc, v139, v73, vcc
	global_load_dwordx4 v[40:43], v[138:139], off offset:-1024
	global_load_dwordx4 v[50:53], v[138:139], off
	v_mul_hi_u32 v129, s25, v78
	v_mad_i32_i24 v130, v129, s24, v78
	v_lshlrev_b32_e32 v128, 2, v129
	v_lshl_add_u32 v131, v130, 7, v128
	v_lshl_add_u32 v131, v74, 2, v131
	v_add_u32_e32 v133, 2, v130
	v_cmp_eq_u32_e32 vcc, s21, v133
	v_lshl_add_u32 v133, v74, 2, v128
	v_add_u32_e32 v133, 4, v133
	v_add_u32_e32 v132, 0x100, v131
	v_and_or_b32 v134, v131, v144, v75
	v_cndmask_b32_e32 v132, v132, v133, vcc
	v_add_u32_e32 v128, 0x80, v131
	v_and_or_b32 v135, v128, v144, v75
	v_and_or_b32 v136, v132, v144, v75
	v_add_u32_e32 v128, 0x80, v132
	v_and_or_b32 v137, v128, v144, v75
	v_max_f32_e32 v100, 0, v100
	v_max_f32_e32 v101, 0, v101
	v_max_f32_e32 v102, 0, v102
	v_max_f32_e32 v103, 0, v103
	v_max_f32_e32 v104, 0, v104
	v_max_f32_e32 v105, 0, v105
	v_max_f32_e32 v106, 0, v106
	v_max_f32_e32 v107, 0, v107
	v_max_f32_e32 v108, 0, v108
	v_max_f32_e32 v109, 0, v109
	v_max_f32_e32 v110, 0, v110
	v_max_f32_e32 v111, 0, v111
	v_max_f32_e32 v112, 0, v112
	v_max_f32_e32 v113, 0, v113
	v_max_f32_e32 v114, 0, v114
	v_max_f32_e32 v115, 0, v115
	v_pk_mul_f32 v[120:121], v[100:101], v[66:67] op_sel_hi:[1,0]
	v_pk_add_f32 v[120:121], v[120:121], 0 op_sel_hi:[1,0]
	v_pk_mul_f32 v[116:117], v[104:105], v[140:141] op_sel_hi:[1,0]
	v_pk_add_f32 v[120:121], v[120:121], v[116:117]
	v_pk_mul_f32 v[116:117], v[108:109], v[68:69] op_sel_hi:[1,0]
	v_pk_add_f32 v[120:121], v[120:121], v[116:117]
	v_pk_mul_f32 v[116:117], v[112:113], v[142:143] op_sel_hi:[1,0]
	v_pk_add_f32 v[120:121], v[120:121], v[116:117]
	v_pk_mul_f32 v[122:123], v[102:103], v[66:67] op_sel_hi:[1,0]
	v_pk_add_f32 v[122:123], v[122:123], 0 op_sel_hi:[1,0]
	v_pk_mul_f32 v[118:119], v[106:107], v[140:141] op_sel_hi:[1,0]
	v_pk_add_f32 v[122:123], v[122:123], v[118:119]
	v_pk_mul_f32 v[118:119], v[110:111], v[68:69] op_sel_hi:[1,0]
	v_pk_add_f32 v[122:123], v[122:123], v[118:119]
	v_pk_mul_f32 v[118:119], v[114:115], v[142:143] op_sel_hi:[1,0]
	v_pk_add_f32 v[122:123], v[122:123], v[118:119]
	v_ashrrev_i32_e32 v128, 31, v120
	v_bitop3_b32 v124, v120, v128, s30 bitop3:0x1e
	ds_write_b32 v134, v124
	v_ashrrev_i32_e32 v128, 31, v121
	v_bitop3_b32 v125, v121, v128, s30 bitop3:0x1e
	ds_write_b32 v135, v125
	v_ashrrev_i32_e32 v128, 31, v122
	v_bitop3_b32 v126, v122, v128, s30 bitop3:0x1e
	ds_write_b32 v136, v126
	v_ashrrev_i32_e32 v128, 31, v123
	v_bitop3_b32 v127, v123, v128, s30 bitop3:0x1e
	ds_write_b32 v137, v127
	s_waitcnt vmcnt(6)
	v_mfma_f32_16x16x32_bf16 v[100:103], v[32:35], v[28:31], 0
	v_mfma_f32_16x16x32_bf16 v[104:107], v[32:35], v[20:23], 0
	v_mfma_f32_16x16x32_bf16 v[108:111], v[32:35], v[12:15], 0
	v_mfma_f32_16x16x32_bf16 v[112:115], v[32:35], v[4:7], 0
	v_mfma_f32_16x16x32_bf16 v[100:103], v[36:39], v[24:27], v[100:103]
	v_mfma_f32_16x16x32_bf16 v[104:107], v[36:39], v[16:19], v[104:107]
	v_mfma_f32_16x16x32_bf16 v[108:111], v[36:39], v[8:11], v[108:111]
	v_mfma_f32_16x16x32_bf16 v[112:115], v[36:39], v[0:3], v[112:115]
	s_add_i32 s28, s5, 56
	s_mov_b32 s29, 0xffff4000
	s_cmp_lt_i32 s28, s19
	s_cselect_b32 s28, 0x10000, s29
	s_cselect_b32 s29, 0, -1
	v_mov_b32_e32 v139, s29
	v_add_co_u32_e32 v138, vcc, s28, v72
	s_nop 1
	v_addc_co_u32_e32 v139, vcc, v139, v73, vcc
	global_load_dwordx4 v[32:35], v[138:139], off offset:-1024
	global_load_dwordx4 v[36:39], v[138:139], off
	v_mul_hi_u32 v129, s25, v77
	v_mad_i32_i24 v130, v129, s24, v77
	v_lshlrev_b32_e32 v128, 2, v129
	v_lshl_add_u32 v131, v130, 7, v128
	v_lshl_add_u32 v131, v74, 2, v131
	v_add_u32_e32 v133, 2, v130
	v_cmp_eq_u32_e32 vcc, s21, v133
	v_lshl_add_u32 v133, v74, 2, v128
	v_add_u32_e32 v133, 4, v133
	v_add_u32_e32 v132, 0x100, v131
	v_and_or_b32 v134, v131, v144, v75
	v_cndmask_b32_e32 v132, v132, v133, vcc
	v_add_u32_e32 v128, 0x80, v131
	v_and_or_b32 v135, v128, v144, v75
	v_and_or_b32 v136, v132, v144, v75
	v_add_u32_e32 v128, 0x80, v132
	v_and_or_b32 v137, v128, v144, v75
	v_max_f32_e32 v100, 0, v100
	v_max_f32_e32 v101, 0, v101
	v_max_f32_e32 v102, 0, v102
	v_max_f32_e32 v103, 0, v103
	v_max_f32_e32 v104, 0, v104
	v_max_f32_e32 v105, 0, v105
	v_max_f32_e32 v106, 0, v106
	v_max_f32_e32 v107, 0, v107
	v_max_f32_e32 v108, 0, v108
	v_max_f32_e32 v109, 0, v109
	v_max_f32_e32 v110, 0, v110
	v_max_f32_e32 v111, 0, v111
	v_max_f32_e32 v112, 0, v112
	v_max_f32_e32 v113, 0, v113
	v_max_f32_e32 v114, 0, v114
	v_max_f32_e32 v115, 0, v115
	v_pk_mul_f32 v[120:121], v[100:101], v[66:67] op_sel_hi:[1,0]
	v_pk_add_f32 v[120:121], v[120:121], 0 op_sel_hi:[1,0]
	v_pk_mul_f32 v[116:117], v[104:105], v[140:141] op_sel_hi:[1,0]
	v_pk_add_f32 v[120:121], v[120:121], v[116:117]
	v_pk_mul_f32 v[116:117], v[108:109], v[68:69] op_sel_hi:[1,0]
	v_pk_add_f32 v[120:121], v[120:121], v[116:117]
	v_pk_mul_f32 v[116:117], v[112:113], v[142:143] op_sel_hi:[1,0]
	v_pk_add_f32 v[120:121], v[120:121], v[116:117]
	v_pk_mul_f32 v[122:123], v[102:103], v[66:67] op_sel_hi:[1,0]
	v_pk_add_f32 v[122:123], v[122:123], 0 op_sel_hi:[1,0]
	v_pk_mul_f32 v[118:119], v[106:107], v[140:141] op_sel_hi:[1,0]
	v_pk_add_f32 v[122:123], v[122:123], v[118:119]
	v_pk_mul_f32 v[118:119], v[110:111], v[68:69] op_sel_hi:[1,0]
	v_pk_add_f32 v[122:123], v[122:123], v[118:119]
	v_pk_mul_f32 v[118:119], v[114:115], v[142:143] op_sel_hi:[1,0]
	v_pk_add_f32 v[122:123], v[122:123], v[118:119]
	v_ashrrev_i32_e32 v128, 31, v120
	v_bitop3_b32 v124, v120, v128, s30 bitop3:0x1e
	ds_write_b32 v134, v124
	v_ashrrev_i32_e32 v128, 31, v121
	v_bitop3_b32 v125, v121, v128, s30 bitop3:0x1e
	ds_write_b32 v135, v125
	v_ashrrev_i32_e32 v128, 31, v122
	v_bitop3_b32 v126, v122, v128, s30 bitop3:0x1e
	ds_write_b32 v136, v126
	v_ashrrev_i32_e32 v128, 31, v123
	v_bitop3_b32 v127, v123, v128, s30 bitop3:0x1e
	ds_write_b32 v137, v127
	s_branch .LBB0_545
.Lmy_ix_last:
	s_waitcnt vmcnt(6)
	v_mfma_f32_16x16x32_bf16 v[100:103], v[62:65], v[28:31], 0
	v_mfma_f32_16x16x32_bf16 v[104:107], v[62:65], v[20:23], 0
	v_mfma_f32_16x16x32_bf16 v[108:111], v[62:65], v[12:15], 0
	v_mfma_f32_16x16x32_bf16 v[112:115], v[62:65], v[4:7], 0
	v_mfma_f32_16x16x32_bf16 v[100:103], v[58:61], v[24:27], v[100:103]
	v_mfma_f32_16x16x32_bf16 v[104:107], v[58:61], v[16:19], v[104:107]
	v_mfma_f32_16x16x32_bf16 v[108:111], v[58:61], v[8:11], v[108:111]
	v_mfma_f32_16x16x32_bf16 v[112:115], v[58:61], v[0:3], v[112:115]
	v_mul_hi_u32 v129, s25, v76
	v_mad_i32_i24 v130, v129, s24, v76
	v_lshlrev_b32_e32 v128, 2, v129
	v_lshl_add_u32 v131, v130, 7, v128
	v_lshl_add_u32 v131, v74, 2, v131
	v_add_u32_e32 v133, 2, v130
	v_cmp_eq_u32_e32 vcc, s21, v133
	v_lshl_add_u32 v133, v74, 2, v128
	v_add_u32_e32 v133, 4, v133
	v_add_u32_e32 v132, 0x100, v131
	v_and_or_b32 v134, v131, v144, v75
	v_cndmask_b32_e32 v132, v132, v133, vcc
	v_add_u32_e32 v128, 0x80, v131
	v_and_or_b32 v135, v128, v144, v75
	v_and_or_b32 v136, v132, v144, v75
	v_add_u32_e32 v128, 0x80, v132
	v_and_or_b32 v137, v128, v144, v75
	v_max_f32_e32 v100, 0, v100
	v_max_f32_e32 v101, 0, v101
	v_max_f32_e32 v102, 0, v102
	v_max_f32_e32 v103, 0, v103
	v_max_f32_e32 v104, 0, v104
	v_max_f32_e32 v105, 0, v105
	v_max_f32_e32 v106, 0, v106
	v_max_f32_e32 v107, 0, v107
	v_max_f32_e32 v108, 0, v108
	v_max_f32_e32 v109, 0, v109
	v_max_f32_e32 v110, 0, v110
	v_max_f32_e32 v111, 0, v111
	v_max_f32_e32 v112, 0, v112
	v_max_f32_e32 v113, 0, v113
	v_max_f32_e32 v114, 0, v114
	v_max_f32_e32 v115, 0, v115
	v_pk_mul_f32 v[120:121], v[100:101], v[66:67] op_sel_hi:[1,0]
	v_pk_add_f32 v[120:121], v[120:121], 0 op_sel_hi:[1,0]
	v_pk_mul_f32 v[116:117], v[104:105], v[140:141] op_sel_hi:[1,0]
	v_pk_add_f32 v[120:121], v[120:121], v[116:117]
	v_pk_mul_f32 v[116:117], v[108:109], v[68:69] op_sel_hi:[1,0]
	v_pk_add_f32 v[120:121], v[120:121], v[116:117]
	v_pk_mul_f32 v[116:117], v[112:113], v[142:143] op_sel_hi:[1,0]
	v_pk_add_f32 v[120:121], v[120:121], v[116:117]
	v_pk_mul_f32 v[122:123], v[102:103], v[66:67] op_sel_hi:[1,0]
	v_pk_add_f32 v[122:123], v[122:123], 0 op_sel_hi:[1,0]
	v_pk_mul_f32 v[118:119], v[106:107], v[140:141] op_sel_hi:[1,0]
	v_pk_add_f32 v[122:123], v[122:123], v[118:119]
	v_pk_mul_f32 v[118:119], v[110:111], v[68:69] op_sel_hi:[1,0]
	v_pk_add_f32 v[122:123], v[122:123], v[118:119]
	v_pk_mul_f32 v[118:119], v[114:115], v[142:143] op_sel_hi:[1,0]
	v_pk_add_f32 v[122:123], v[122:123], v[118:119]
	v_ashrrev_i32_e32 v128, 31, v120
	v_bitop3_b32 v124, v120, v128, s30 bitop3:0x1e
	ds_write_b32 v134, v124
	v_ashrrev_i32_e32 v128, 31, v121
	v_bitop3_b32 v125, v121, v128, s30 bitop3:0x1e
	ds_write_b32 v135, v125
	v_ashrrev_i32_e32 v128, 31, v122
	v_bitop3_b32 v126, v122, v128, s30 bitop3:0x1e
	ds_write_b32 v136, v126
	v_ashrrev_i32_e32 v128, 31, v123
	v_bitop3_b32 v127, v123, v128, s30 bitop3:0x1e
	ds_write_b32 v137, v127
	s_add_i32 s28, s5, 8
	s_cmp_lt_i32 s28, s19
	s_cbranch_scc0 .Lmy_ix_end
	s_waitcnt vmcnt(4)
	v_mfma_f32_16x16x32_bf16 v[100:103], v[44:47], v[28:31], 0
	v_mfma_f32_16x16x32_bf16 v[104:107], v[44:47], v[20:23], 0
	v_mfma_f32_16x16x32_bf16 v[108:111], v[44:47], v[12:15], 0
	v_mfma_f32_16x16x32_bf16 v[112:115], v[44:47], v[4:7], 0
	v_mfma_f32_16x16x32_bf16 v[100:103], v[54:57], v[24:27], v[100:103]
	v_mfma_f32_16x16x32_bf16 v[104:107], v[54:57], v[16:19], v[104:107]
	v_mfma_f32_16x16x32_bf16 v[108:111], v[54:57], v[8:11], v[108:111]
	v_mfma_f32_16x16x32_bf16 v[112:115], v[54:57], v[0:3], v[112:115]
	v_mul_hi_u32 v129, s25, v79
	v_mad_i32_i24 v130, v129, s24, v79
	v_lshlrev_b32_e32 v128, 2, v129
	v_lshl_add_u32 v131, v130, 7, v128
	v_lshl_add_u32 v131, v74, 2, v131
	v_add_u32_e32 v133, 2, v130
	v_cmp_eq_u32_e32 vcc, s21, v133
	v_lshl_add_u32 v133, v74, 2, v128
	v_add_u32_e32 v133, 4, v133
	v_add_u32_e32 v132, 0x100, v131
	v_and_or_b32 v134, v131, v144, v75
	v_cndmask_b32_e32 v132, v132, v133, vcc
	v_add_u32_e32 v128, 0x80, v131
	v_and_or_b32 v135, v128, v144, v75
	v_and_or_b32 v136, v132, v144, v75
	v_add_u32_e32 v128, 0x80, v132
	v_and_or_b32 v137, v128, v144, v75
	v_max_f32_e32 v100, 0, v100
	v_max_f32_e32 v101, 0, v101
	v_max_f32_e32 v102, 0, v102
	v_max_f32_e32 v103, 0, v103
	v_max_f32_e32 v104, 0, v104
	v_max_f32_e32 v105, 0, v105
	v_max_f32_e32 v106, 0, v106
	v_max_f32_e32 v107, 0, v107
	v_max_f32_e32 v108, 0, v108
	v_max_f32_e32 v109, 0, v109
	v_max_f32_e32 v110, 0, v110
	v_max_f32_e32 v111, 0, v111
	v_max_f32_e32 v112, 0, v112
	v_max_f32_e32 v113, 0, v113
	v_max_f32_e32 v114, 0, v114
	v_max_f32_e32 v115, 0, v115
	v_pk_mul_f32 v[120:121], v[100:101], v[66:67] op_sel_hi:[1,0]
	v_pk_add_f32 v[120:121], v[120:121], 0 op_sel_hi:[1,0]
	v_pk_mul_f32 v[116:117], v[104:105], v[140:141] op_sel_hi:[1,0]
	v_pk_add_f32 v[120:121], v[120:121], v[116:117]
	v_pk_mul_f32 v[116:117], v[108:109], v[68:69] op_sel_hi:[1,0]
	v_pk_add_f32 v[120:121], v[120:121], v[116:117]
	v_pk_mul_f32 v[116:117], v[112:113], v[142:143] op_sel_hi:[1,0]
	v_pk_add_f32 v[120:121], v[120:121], v[116:117]
	v_pk_mul_f32 v[122:123], v[102:103], v[66:67] op_sel_hi:[1,0]
	v_pk_add_f32 v[122:123], v[122:123], 0 op_sel_hi:[1,0]
	v_pk_mul_f32 v[118:119], v[106:107], v[140:141] op_sel_hi:[1,0]
	v_pk_add_f32 v[122:123], v[122:123], v[118:119]
	v_pk_mul_f32 v[118:119], v[110:111], v[68:69] op_sel_hi:[1,0]
	v_pk_add_f32 v[122:123], v[122:123], v[118:119]
	v_pk_mul_f32 v[118:119], v[114:115], v[142:143] op_sel_hi:[1,0]
	v_pk_add_f32 v[122:123], v[122:123], v[118:119]
	v_ashrrev_i32_e32 v128, 31, v120
	v_bitop3_b32 v124, v120, v128, s30 bitop3:0x1e
	ds_write_b32 v134, v124
	v_ashrrev_i32_e32 v128, 31, v121
	v_bitop3_b32 v125, v121, v128, s30 bitop3:0x1e
	ds_write_b32 v135, v125
	v_ashrrev_i32_e32 v128, 31, v122
	v_bitop3_b32 v126, v122, v128, s30 bitop3:0x1e
	ds_write_b32 v136, v126
	v_ashrrev_i32_e32 v128, 31, v123
	v_bitop3_b32 v127, v123, v128, s30 bitop3:0x1e
	ds_write_b32 v137, v127
	s_add_i32 s28, s5, 16
	s_cmp_lt_i32 s28, s19
	s_cbranch_scc0 .Lmy_ix_end
	s_waitcnt vmcnt(2)
	v_mfma_f32_16x16x32_bf16 v[100:103], v[40:43], v[28:31], 0
	v_mfma_f32_16x16x32_bf16 v[104:107], v[40:43], v[20:23], 0
	v_mfma_f32_16x16x32_bf16 v[108:111], v[40:43], v[12:15], 0
	v_mfma_f32_16x16x32_bf16 v[112:115], v[40:43], v[4:7], 0
	v_mfma_f32_16x16x32_bf16 v[100:103], v[50:53], v[24:27], v[100:103]
	v_mfma_f32_16x16x32_bf16 v[104:107], v[50:53], v[16:19], v[104:107]
	v_mfma_f32_16x16x32_bf16 v[108:111], v[50:53], v[8:11], v[108:111]
	v_mfma_f32_16x16x32_bf16 v[112:115], v[50:53], v[0:3], v[112:115]
	v_mul_hi_u32 v129, s25, v78
	v_mad_i32_i24 v130, v129, s24, v78
	v_lshlrev_b32_e32 v128, 2, v129
	v_lshl_add_u32 v131, v130, 7, v128
	v_lshl_add_u32 v131, v74, 2, v131
	v_add_u32_e32 v133, 2, v130
	v_cmp_eq_u32_e32 vcc, s21, v133
	v_lshl_add_u32 v133, v74, 2, v128
	v_add_u32_e32 v133, 4, v133
	v_add_u32_e32 v132, 0x100, v131
	v_and_or_b32 v134, v131, v144, v75
	v_cndmask_b32_e32 v132, v132, v133, vcc
	v_add_u32_e32 v128, 0x80, v131
	v_and_or_b32 v135, v128, v144, v75
	v_and_or_b32 v136, v132, v144, v75
	v_add_u32_e32 v128, 0x80, v132
	v_and_or_b32 v137, v128, v144, v75
	v_max_f32_e32 v100, 0, v100
	v_max_f32_e32 v101, 0, v101
	v_max_f32_e32 v102, 0, v102
	v_max_f32_e32 v103, 0, v103
	v_max_f32_e32 v104, 0, v104
	v_max_f32_e32 v105, 0, v105
	v_max_f32_e32 v106, 0, v106
	v_max_f32_e32 v107, 0, v107
	v_max_f32_e32 v108, 0, v108
	v_max_f32_e32 v109, 0, v109
	v_max_f32_e32 v110, 0, v110
	v_max_f32_e32 v111, 0, v111
	v_max_f32_e32 v112, 0, v112
	v_max_f32_e32 v113, 0, v113
	v_max_f32_e32 v114, 0, v114
	v_max_f32_e32 v115, 0, v115
	v_pk_mul_f32 v[120:121], v[100:101], v[66:67] op_sel_hi:[1,0]
	v_pk_add_f32 v[120:121], v[120:121], 0 op_sel_hi:[1,0]
	v_pk_mul_f32 v[116:117], v[104:105], v[140:141] op_sel_hi:[1,0]
	v_pk_add_f32 v[120:121], v[120:121], v[116:117]
	v_pk_mul_f32 v[116:117], v[108:109], v[68:69] op_sel_hi:[1,0]
	v_pk_add_f32 v[120:121], v[120:121], v[116:117]
	v_pk_mul_f32 v[116:117], v[112:113], v[142:143] op_sel_hi:[1,0]
	v_pk_add_f32 v[120:121], v[120:121], v[116:117]
	v_pk_mul_f32 v[122:123], v[102:103], v[66:67] op_sel_hi:[1,0]
	v_pk_add_f32 v[122:123], v[122:123], 0 op_sel_hi:[1,0]
	v_pk_mul_f32 v[118:119], v[106:107], v[140:141] op_sel_hi:[1,0]
	v_pk_add_f32 v[122:123], v[122:123], v[118:119]
	v_pk_mul_f32 v[118:119], v[110:111], v[68:69] op_sel_hi:[1,0]
	v_pk_add_f32 v[122:123], v[122:123], v[118:119]
	v_pk_mul_f32 v[118:119], v[114:115], v[142:143] op_sel_hi:[1,0]
	v_pk_add_f32 v[122:123], v[122:123], v[118:119]
	v_ashrrev_i32_e32 v128, 31, v120
	v_bitop3_b32 v124, v120, v128, s30 bitop3:0x1e
	ds_write_b32 v134, v124
	v_ashrrev_i32_e32 v128, 31, v121
	v_bitop3_b32 v125, v121, v128, s30 bitop3:0x1e
	ds_write_b32 v135, v125
	v_ashrrev_i32_e32 v128, 31, v122
	v_bitop3_b32 v126, v122, v128, s30 bitop3:0x1e
	ds_write_b32 v136, v126
	v_ashrrev_i32_e32 v128, 31, v123
	v_bitop3_b32 v127, v123, v128, s30 bitop3:0x1e
	ds_write_b32 v137, v127
	s_add_i32 s28, s5, 24
	s_cmp_lt_i32 s28, s19
	s_cbranch_scc0 .Lmy_ix_end
	s_waitcnt vmcnt(0)
	v_mfma_f32_16x16x32_bf16 v[100:103], v[32:35], v[28:31], 0
	v_mfma_f32_16x16x32_bf16 v[104:107], v[32:35], v[20:23], 0
	v_mfma_f32_16x16x32_bf16 v[108:111], v[32:35], v[12:15], 0
	v_mfma_f32_16x16x32_bf16 v[112:115], v[32:35], v[4:7], 0
	v_mfma_f32_16x16x32_bf16 v[100:103], v[36:39], v[24:27], v[100:103]
	v_mfma_f32_16x16x32_bf16 v[104:107], v[36:39], v[16:19], v[104:107]
	v_mfma_f32_16x16x32_bf16 v[108:111], v[36:39], v[8:11], v[108:111]
	v_mfma_f32_16x16x32_bf16 v[112:115], v[36:39], v[0:3], v[112:115]
	v_mul_hi_u32 v129, s25, v77
	v_mad_i32_i24 v130, v129, s24, v77
	v_lshlrev_b32_e32 v128, 2, v129
	v_lshl_add_u32 v131, v130, 7, v128
	v_lshl_add_u32 v131, v74, 2, v131
	v_add_u32_e32 v133, 2, v130
	v_cmp_eq_u32_e32 vcc, s21, v133
	v_lshl_add_u32 v133, v74, 2, v128
	v_add_u32_e32 v133, 4, v133
	v_add_u32_e32 v132, 0x100, v131
	v_and_or_b32 v134, v131, v144, v75
	v_cndmask_b32_e32 v132, v132, v133, vcc
	v_add_u32_e32 v128, 0x80, v131
	v_and_or_b32 v135, v128, v144, v75
	v_and_or_b32 v136, v132, v144, v75
	v_add_u32_e32 v128, 0x80, v132
	v_and_or_b32 v137, v128, v144, v75
	v_max_f32_e32 v100, 0, v100
	v_max_f32_e32 v101, 0, v101
	v_max_f32_e32 v102, 0, v102
	v_max_f32_e32 v103, 0, v103
	v_max_f32_e32 v104, 0, v104
	v_max_f32_e32 v105, 0, v105
	v_max_f32_e32 v106, 0, v106
	v_max_f32_e32 v107, 0, v107
	v_max_f32_e32 v108, 0, v108
	v_max_f32_e32 v109, 0, v109
	v_max_f32_e32 v110, 0, v110
	v_max_f32_e32 v111, 0, v111
	v_max_f32_e32 v112, 0, v112
	v_max_f32_e32 v113, 0, v113
	v_max_f32_e32 v114, 0, v114
	v_max_f32_e32 v115, 0, v115
	v_pk_mul_f32 v[120:121], v[100:101], v[66:67] op_sel_hi:[1,0]
	v_pk_add_f32 v[120:121], v[120:121], 0 op_sel_hi:[1,0]
	v_pk_mul_f32 v[116:117], v[104:105], v[140:141] op_sel_hi:[1,0]
	v_pk_add_f32 v[120:121], v[120:121], v[116:117]
	v_pk_mul_f32 v[116:117], v[108:109], v[68:69] op_sel_hi:[1,0]
	v_pk_add_f32 v[120:121], v[120:121], v[116:117]
	v_pk_mul_f32 v[116:117], v[112:113], v[142:143] op_sel_hi:[1,0]
	v_pk_add_f32 v[120:121], v[120:121], v[116:117]
	v_pk_mul_f32 v[122:123], v[102:103], v[66:67] op_sel_hi:[1,0]
	v_pk_add_f32 v[122:123], v[122:123], 0 op_sel_hi:[1,0]
	v_pk_mul_f32 v[118:119], v[106:107], v[140:141] op_sel_hi:[1,0]
	v_pk_add_f32 v[122:123], v[122:123], v[118:119]
	v_pk_mul_f32 v[118:119], v[110:111], v[68:69] op_sel_hi:[1,0]
	v_pk_add_f32 v[122:123], v[122:123], v[118:119]
	v_pk_mul_f32 v[118:119], v[114:115], v[142:143] op_sel_hi:[1,0]
	v_pk_add_f32 v[122:123], v[122:123], v[118:119]
	v_ashrrev_i32_e32 v128, 31, v120
	v_bitop3_b32 v124, v120, v128, s30 bitop3:0x1e
	ds_write_b32 v134, v124
	v_ashrrev_i32_e32 v128, 31, v121
	v_bitop3_b32 v125, v121, v128, s30 bitop3:0x1e
	ds_write_b32 v135, v125
	v_ashrrev_i32_e32 v128, 31, v122
	v_bitop3_b32 v126, v122, v128, s30 bitop3:0x1e
	ds_write_b32 v136, v126
	v_ashrrev_i32_e32 v128, 31, v123
	v_bitop3_b32 v127, v123, v128, s30 bitop3:0x1e
	ds_write_b32 v137, v127
